# waves 4-7: K-loop final barrier moved past the unit switch (decode + accumulator zeroing) to the next unit's preheader end; pending flag in s100
# speedup vs baseline: 1.0096x; 1.0011x over previous
;     __device__ bool next(int i, Unit& u) const {
;         const long L = (long)i * G + c;
;         const int x = (int)(L - nwg); const bool tail = L >= nwg;
;         if (tail && (ksplit <= 1 || x >= nN * ksplit)) return false;
;         int wgid = tail ? 0 : (int)L; { const int q = nwg / NXCD, r = nwg % NXCD, xcd = wgid % NXCD, off = wgid / NXCD; wgid = (xcd < r ? xcd * (q + 1) : r * (q + 1) + (xcd - r) * q) + off; }
;         const int nig = WGM * nN, gid = wgid / nig, fm = gid * WGM, gsz = (nM - fm) < WGM ? (nM - fm) : WGM;
;         const int ks = tail ? x / nN : 0;
;         u.row0 = tail ? nM * BM : (fm + ((wgid % nig) % gsz)) * BM; u.pn = tail ? x % nN : (wgid % nig) / gsz; u.rend = M; u.e = ks;
;         u.koff = tail ? ks * (K / ksplit) : 0; u.kt = tail ? K / ksplit / BK : K / BK; u.loff = 0; return true;
.LBB0_107:
	s_mov_b32 s100, 0
	s_mov_b32 s36, s65
	s_mov_b64 s[8:9], s[66:67]
	v_writelane_b32 v255, s28, 8
	s_waitcnt vmcnt(6)
	v_mbcnt_lo_u32_b32 v6, -1, 0
	v_mbcnt_hi_u32_b32 v6, -1, v6
	s_cmpk_lt_i32 s36, 0x58b
	v_or_b32_e32 v0, s75, v6
	v_writelane_b32 v255, s29, 9
	s_cselect_b64 s[0:1], -1, 0
	s_cmpk_gt_i32 s36, 0x58a
	v_readfirstlane_b32 s37, v0
	s_cbranch_scc1 .LBB0_113
	s_ashr_i32 s2, s36, 31
	s_lshr_b32 s2, s2, 29
	s_add_i32 s4, s36, s2
	s_and_b32 s2, s4, -8
	s_sub_i32 s5, s36, s2
	s_cmp_gt_i32 s5, 2
	s_mov_b64 s[2:3], -1
	s_cbranch_scc0 .LBB0_110
	s_mul_i32 s2, s5, 0xb1
	s_add_i32 s6, s2, 3
	s_mov_b64 s[2:3], 0

; template <class Epi, class Sched>
; __device__ __forceinline__ void gemm_phase(LAS unsigned char* lds, const bf16_t* Abase, const int K, const Sched& S, const Epi& E, const int wvid) {
;     ...
;         E(acc, cur, wr, wc, fr, fq);
;         if (!has_next) break;
; #pragma unroll
;         for (int a = 0; a < 2; ++a)
; #pragma unroll
;             for (int b = 0; b < 2; ++b)
; #pragma unroll
;                 for (int m = 0; m < 4; ++m)
; #pragma unroll
;                     for (int n = 0; n < 2; ++n) acc[a][b][m][n] = (f32x4){0.f, 0.f, 0.f, 0.f};
;         cur = nxt; cB = nB; ++ui;
.LBB0_117:
	s_or_b64 exec, exec, s[28:29]
	s_mov_b32 s100, 1
	s_and_b64 vcc, exec, s[2:3]
	s_mov_b32 s57, s56
	s_mov_b32 s16, s24
	s_mov_b64 s[4:5], s[26:27]
	s_cbranch_vccnz .LBB0_202

;     __device__ __forceinline__ const char* b_ptr(const Unit& u) const { return (const char*)Bt + ((size_t)u.pn * BM * K + u.koff) * 2; }
;     __device__ __forceinline__ const char* b_ptr(const Unit& u) const { return (const char*)Bt + ((size_t)u.e * bstride + (size_t)u.pn * BM * K) * 2; }
; #define PG8_STAGE(bufoff, gbase, voff) do { _Pragma("unroll") for (int _i = 0; _i < 2; ++_i) \
;         __builtin_amdgcn_global_load_lds((const unsigned*)((const char*)(gbase) + (voff)[_i]), (LAS unsigned*)(lds + (bufoff) + ldsw + _i * 8192), 16, 0, 0); } while (0)
; #define PG8_LDA(dst, b, h) do { _Pragma("unroll") for (int m = 0; m < 4; ++m) _Pragma("unroll") for (int k = 0; k < 2; ++k) dst[m][k] = *(const LAS bf16x8*)(lds + PG8_SA(b, h) + aoff + m * 2048 + k * 1024); } while (0)
; #define PG8_LDB(dst, b, h) do { _Pragma("unroll") for (int n = 0; n < 2; ++n) _Pragma("unroll") for (int k = 0; k < 2; ++k) dst[n][k] = *(const LAS bf16x8*)(lds + PG8_SB(b, h) + boff + n * 2048 + k * 1024); } while (0)
; #define PG8_WAIT_L(n) asm volatile("s_waitcnt lgkmcnt(" #n ")" ::: "memory")
; #define PG8_BAR __builtin_amdgcn_s_barrier()
; #define PG8_SCHED __builtin_amdgcn_sched_barrier(0)
; template <class Epi, class Sched>
; __device__ __forceinline__ void gemm_phase(LAS unsigned char* lds, const bf16_t* Abase, const int K, const Sched& S, const Epi& E, const int wvid) {
;     ...
;         const bool has_next = S.next(ui + 1, nxt);
;         const char* nB = has_next ? S.b_ptr(nxt) : cB;
;         const int nt = cur.kt;
;         for (int t = 0; t < nt; t += 2) {
;             const bool last = (t == nt - 2);
;             const char* a1 = Ab + (size_t)(t + 1) * kstep;
;             PG8_LDB(B0, 0, 0); PG8_SCHED; PG8_LDA(At, 0, 0); PG8_STAGE(PG8_SA(1, 1), a1, voffA[1]);
;             PG8_WAIT_L(8); PG8_BAR; PG8_WAIT_L(0); PG8_MMA(0, 0, At, B0); PG8_BAR; PG8_SCHED;
;             if (last && has_next) PG8_AOFF(nxt);
;     ...
; #pragma unroll
;         for (int a = 0; a < 2; ++a)
; #pragma unroll
;             for (int b = 0; b < 2; ++b)
; #pragma unroll
;                 for (int m = 0; m < 4; ++m)
; #pragma unroll
;                     for (int n = 0; n < 2; ++n) acc[a][b][m][n] = (f32x4){0.f, 0.f, 0.f, 0.f};
;         cur = nxt; cB = nB; ++ui;
.LBB0_124:
	s_ashr_i32 s25, s24, 31
	s_lshl_b64 s[26:27], s[24:25], 19
	s_add_u32 s26, s38, s26
	s_addc_u32 s27, s39, s27
	s_and_b64 s[28:29], s[0:1], exec
	s_cselect_b32 s25, s27, s5
	s_cselect_b32 s58, s26, s4
	s_add_u32 s59, s4, 0x100
	v_mov_b32_e32 v2, 0
	s_addc_u32 s60, s5, 0
	s_mov_b32 s61, -2
	s_mov_b64 s[4:5], 0
	v_mov_b32_e32 v3, v2
	v_mov_b64_e32 v[4:5], 0
	v_mov_b64_e32 v[6:7], 0
	v_mov_b64_e32 v[8:9], 0
	v_mov_b64_e32 v[18:19], 0
	v_mov_b64_e32 v[20:21], 0
	v_mov_b64_e32 v[22:23], 0
	v_mov_b64_e32 v[24:25], 0
	v_mov_b64_e32 v[34:35], 0
	v_mov_b64_e32 v[36:37], 0
	v_mov_b64_e32 v[38:39], 0
	v_mov_b64_e32 v[40:41], 0
	v_mov_b64_e32 v[50:51], 0
	v_mov_b64_e32 v[52:53], 0
	v_mov_b64_e32 v[54:55], 0
	v_mov_b64_e32 v[56:57], 0
	v_mov_b64_e32 v[10:11], 0
	v_mov_b64_e32 v[12:13], 0
	v_mov_b64_e32 v[14:15], 0
	v_mov_b64_e32 v[16:17], 0
	v_mov_b64_e32 v[26:27], 0
	v_mov_b64_e32 v[28:29], 0
	v_mov_b64_e32 v[30:31], 0
	v_mov_b64_e32 v[32:33], 0
	v_mov_b64_e32 v[42:43], 0
	v_mov_b64_e32 v[44:45], 0
	v_mov_b64_e32 v[46:47], 0
	v_mov_b64_e32 v[48:49], 0
	v_mov_b64_e32 v[58:59], 0
	v_mov_b64_e32 v[60:61], 0
	v_mov_b64_e32 v[62:63], 0
	v_mov_b64_e32 v[64:65], 0
	v_mov_b64_e32 v[66:67], 0
	v_mov_b64_e32 v[68:69], 0
	v_mov_b64_e32 v[70:71], 0
	v_mov_b64_e32 v[72:73], 0
	v_mov_b64_e32 v[74:75], 0
	v_mov_b64_e32 v[76:77], 0
	v_mov_b64_e32 v[78:79], 0
	v_mov_b64_e32 v[80:81], 0
	v_mov_b64_e32 v[90:91], 0
	v_mov_b64_e32 v[92:93], 0
	v_mov_b64_e32 v[94:95], 0
	v_mov_b64_e32 v[96:97], 0
	v_mov_b64_e32 v[106:107], 0
	v_mov_b64_e32 v[108:109], 0
	v_mov_b64_e32 v[110:111], 0
	v_mov_b64_e32 v[112:113], 0
	v_mov_b64_e32 v[82:83], 0
	v_mov_b64_e32 v[84:85], 0
	v_mov_b64_e32 v[86:87], 0
	v_mov_b64_e32 v[88:89], 0
	v_mov_b64_e32 v[98:99], 0
	v_mov_b64_e32 v[100:101], 0
	v_mov_b64_e32 v[102:103], 0
	v_mov_b64_e32 v[104:105], 0
	v_mov_b64_e32 v[114:115], 0
	v_mov_b64_e32 v[116:117], 0
	v_mov_b64_e32 v[118:119], 0
	v_mov_b64_e32 v[120:121], 0
	v_mov_b64_e32 v[122:123], 0
	v_mov_b64_e32 v[124:125], 0
	v_mov_b64_e32 v[126:127], 0
	v_mov_b64_e32 v[128:129], 0
	s_cmp_lt_u32 s74, 0x100
	s_cbranch_scc1 .Lz0
	s_cmp_eq_u32 s100, 0
	s_cbranch_scc1 .Lz0
	s_barrier
.Lz0:
.LBB0_125:
	ds_read_b128 v[130:133], v193
	ds_read_b128 v[134:137], v193 offset:1024
	ds_read_b128 v[138:141], v193 offset:2048
	ds_read_b128 v[142:145], v193 offset:3072
	s_cmp_eq_u32 s61, 12
	s_cselect_b64 s[30:31], -1, 0
	s_add_i32 m0, s17, 0xc000
	s_add_u32 s28, s22, s4
	s_addc_u32 s29, s23, s5
	ds_read_b128 v[170:173], v194
	ds_read_b128 v[174:177], v194 offset:1024
	ds_read_b128 v[162:165], v194 offset:2048
	ds_read_b128 v[166:169], v194 offset:3072
	ds_read_b128 v[154:157], v194 offset:4096
	ds_read_b128 v[158:161], v194 offset:5120
	ds_read_b128 v[146:149], v194 offset:6144
	ds_read_b128 v[150:153], v194 offset:7168
	global_load_lds_dwordx4 v182, s[28:29]
	s_add_i32 m0, s17, 0xe000
	s_nop 0
	global_load_lds_dwordx4 v186, s[28:29]
	s_waitcnt lgkmcnt(8)
	s_barrier
	s_waitcnt lgkmcnt(0)
	s_waitcnt lgkmcnt(0)
	v_mfma_f32_16x16x32_bf16 v[126:129], v[130:133], v[170:173], v[126:129]
	v_mfma_f32_16x16x32_bf16 v[122:125], v[138:141], v[170:173], v[122:125]
	v_mfma_f32_16x16x32_bf16 v[118:121], v[130:133], v[162:165], v[118:121]
	v_mfma_f32_16x16x32_bf16 v[114:117], v[138:141], v[162:165], v[114:117]
	v_mfma_f32_16x16x32_bf16 v[102:105], v[130:133], v[154:157], v[102:105]
	v_mfma_f32_16x16x32_bf16 v[98:101], v[138:141], v[154:157], v[98:101]
	v_mfma_f32_16x16x32_bf16 v[86:89], v[130:133], v[146:149], v[86:89]
	v_mfma_f32_16x16x32_bf16 v[82:85], v[138:141], v[146:149], v[82:85]
	v_mfma_f32_16x16x32_bf16 v[126:129], v[134:137], v[174:177], v[126:129]
	v_mfma_f32_16x16x32_bf16 v[122:125], v[142:145], v[174:177], v[122:125]
	v_mfma_f32_16x16x32_bf16 v[118:121], v[134:137], v[166:169], v[118:121]
	v_mfma_f32_16x16x32_bf16 v[114:117], v[142:145], v[166:169], v[114:117]
	v_mfma_f32_16x16x32_bf16 v[102:105], v[134:137], v[158:161], v[102:105]
	v_mfma_f32_16x16x32_bf16 v[98:101], v[142:145], v[158:161], v[98:101]
	v_mfma_f32_16x16x32_bf16 v[86:89], v[134:137], v[150:153], v[86:89]
	v_mfma_f32_16x16x32_bf16 v[82:85], v[142:145], v[150:153], v[82:85]
	s_barrier
	s_and_b64 s[28:29], s[0:1], s[30:31]
	s_andn2_b64 vcc, exec, s[28:29]
	s_cbranch_vccnz .LBB0_127
	v_mbcnt_lo_u32_b32 v0, -1, 0
	v_mbcnt_hi_u32_b32 v0, -1, v0
	s_nop 0
	v_or_b32_e32 v0, s75, v0
	v_ashrrev_i32_e32 v183, 31, v0
	v_lshrrev_b32_e32 v183, 26, v183
	v_lshlrev_b32_e32 v182, 4, v0
	v_add_u32_e32 v183, v0, v183
	v_bfe_i32 v0, v0, 27, 1
	v_lshrrev_b32_e32 v0, 22, v0
	v_add_u32_e32 v0, v182, v0
	v_and_b32_e32 v0, 0xfffffc00, v0
	v_sub_u32_e32 v0, v182, v0
	v_lshrrev_b32_e32 v184, 4, v0
	v_bitop3_b32 v0, v184, v0, 32 bitop3:0x6c
	v_ashrrev_i32_e32 v185, 31, v0
	v_lshrrev_b32_e32 v185, 26, v185
	v_ashrrev_i32_e32 v183, 6, v183
	v_add_u32_e32 v185, v0, v185
	v_lshlrev_b32_e32 v184, 3, v183
	v_lshrrev_b32_e32 v186, 6, v185
	v_and_b32_e32 v185, 0xc0, v185
	v_and_b32_e32 v184, 0x1ffff0, v184
	v_lshlrev_b32_e32 v183, 5, v183
	v_sub_u32_e32 v0, v0, v185
	v_and_b32_e32 v183, 32, v183
	v_ashrrev_i16_sdwa v0, v216, sext(v0) dst_sel:DWORD dst_unused:UNUSED_PAD src0_sel:DWORD src1_sel:BYTE_0
	v_add_u32_e32 v184, s56, v184
	v_add_u32_e32 v182, 0x2000, v182
	v_add_u32_sdwa v0, v183, sext(v0) dst_sel:DWORD dst_unused:UNUSED_PAD src0_sel:DWORD src1_sel:WORD_0
	v_add_lshl_u32 v183, v184, v186, 11
	v_ashrrev_i32_e32 v184, 31, v182
	v_lshrrev_b32_e32 v184, 22, v184
	v_add_u32_e32 v184, v182, v184
	v_ashrrev_i32_e32 v184, 10, v184
	v_mul_i32_i24_e32 v185, 0x400, v184
	v_sub_u32_e32 v182, v182, v185
	v_lshrrev_b32_e32 v185, 4, v182
	v_bitop3_b32 v182, v185, v182, 32 bitop3:0x6c
	v_ashrrev_i32_e32 v186, 31, v182
	v_lshrrev_b32_e32 v186, 26, v186
	v_add_u32_e32 v186, v182, v186
	v_lshlrev_b32_e32 v185, 3, v184
	v_lshrrev_b32_e32 v187, 6, v186
	v_and_b32_e32 v186, 0xc0, v186
	v_and_b32_e32 v185, 0x1ffff0, v185
	v_lshlrev_b32_e32 v184, 5, v184
	v_sub_u32_e32 v182, v182, v186
	v_and_b32_e32 v184, 32, v184
	v_ashrrev_i16_sdwa v182, v216, sext(v182) dst_sel:DWORD dst_unused:UNUSED_PAD src0_sel:DWORD src1_sel:BYTE_0
	v_add_u32_e32 v185, s56, v185
	v_lshl_add_u32 v183, v0, 1, v183
	v_add_u32_sdwa v182, v184, sext(v182) dst_sel:DWORD dst_unused:UNUSED_PAD src0_sel:DWORD src1_sel:WORD_0
	v_add_lshl_u32 v184, v185, v187, 11
	v_add_u32_e32 v0, 0x40000, v183
	v_lshl_add_u32 v184, v182, 1, v184
	v_add_u32_e32 v186, 0x40000, v184
	v_mov_b32_e32 v187, v1
	v_mov_b64_e32 v[188:189], v[0:1]
	v_mov_b32_e32 v182, v0
	v_mov_b32_e32 v0, v183
	s_branch .LBB0_128

; #define PG8_WAIT_V(n) asm volatile("s_waitcnt vmcnt(" #n ")" ::: "memory")
; #define PG8_BAR __builtin_amdgcn_s_barrier()
; template <class Epi, class Sched>
; __device__ __forceinline__ void gemm_phase(LAS unsigned char* lds, const bf16_t* Abase, const int K, const Sched& S, const Epi& E, const int wvid) {
;     ...
;     PG8_WAIT_V(0);
;     if (wr == 0) PG8_BAR;
;     PG8_BAR;
.LBB0_202:
	s_cmp_lt_u32 s74, 0x100
	s_cbranch_scc1 .Lw0
	s_cmp_eq_u32 s100, 0
	s_cbranch_scc1 .Lw0
	s_barrier
.Lw0:
	s_mov_b32 s100, 0
	s_waitcnt vmcnt(0)
	s_cmpk_gt_u32 s37, 0xff
	s_cbranch_scc1 .LBB0_204
	s_barrier

; template <class Epi, class Sched>
; __device__ __forceinline__ void gemm_phase(LAS unsigned char* lds, const bf16_t* Abase, const int K, const Sched& S, const Epi& E, const int wvid) {
;     ...
;         E(acc, cur, wr, wc, fr, fq);
;         if (!has_next) break;
; #pragma unroll
;         for (int a = 0; a < 2; ++a)
; #pragma unroll
;             for (int b = 0; b < 2; ++b)
; #pragma unroll
;                 for (int m = 0; m < 4; ++m)
; #pragma unroll
;                     for (int n = 0; n < 2; ++n) acc[a][b][m][n] = (f32x4){0.f, 0.f, 0.f, 0.f};
;         cur = nxt; cB = nB; ++ui;
.LBB0_987:
	s_mov_b32 s100, 1
	s_and_b64 vcc, exec, s[20:21]
	s_mov_b32 s9, s55
	s_mov_b32 s22, s10
	s_mov_b32 s8, s56
	s_mov_b32 s57, s54
	s_mov_b64 s[26:27], s[18:19]
	s_cbranch_vccnz .LBB0_1011

;     __device__ __forceinline__ const char* b_ptr(const Unit& u) const { return (const char*)Bt + ((size_t)u.pn * BM * K + u.koff) * 2; }
;     __device__ __forceinline__ const char* b_ptr(const Unit& u) const { return (const char*)Bt + ((size_t)u.e * bstride + (size_t)u.pn * BM * K) * 2; }
; #define PG8_STAGE(bufoff, gbase, voff) do { _Pragma("unroll") for (int _i = 0; _i < 2; ++_i) \
;         __builtin_amdgcn_global_load_lds((const unsigned*)((const char*)(gbase) + (voff)[_i]), (LAS unsigned*)(lds + (bufoff) + ldsw + _i * 8192), 16, 0, 0); } while (0)
; #define PG8_LDA(dst, b, h) do { _Pragma("unroll") for (int m = 0; m < 4; ++m) _Pragma("unroll") for (int k = 0; k < 2; ++k) dst[m][k] = *(const LAS bf16x8*)(lds + PG8_SA(b, h) + aoff + m * 2048 + k * 1024); } while (0)
; #define PG8_LDB(dst, b, h) do { _Pragma("unroll") for (int n = 0; n < 2; ++n) _Pragma("unroll") for (int k = 0; k < 2; ++k) dst[n][k] = *(const LAS bf16x8*)(lds + PG8_SB(b, h) + boff + n * 2048 + k * 1024); } while (0)
; #define PG8_WAIT_L(n) asm volatile("s_waitcnt lgkmcnt(" #n ")" ::: "memory")
; #define PG8_BAR __builtin_amdgcn_s_barrier()
; #define PG8_SCHED __builtin_amdgcn_sched_barrier(0)
; template <class Epi, class Sched>
; __device__ __forceinline__ void gemm_phase(LAS unsigned char* lds, const bf16_t* Abase, const int K, const Sched& S, const Epi& E, const int wvid) {
;     ...
;         const bool has_next = S.next(ui + 1, nxt);
;         const char* nB = has_next ? S.b_ptr(nxt) : cB;
;         const int nt = cur.kt;
;         for (int t = 0; t < nt; t += 2) {
;             const bool last = (t == nt - 2);
;             const char* a1 = Ab + (size_t)(t + 1) * kstep;
;             PG8_LDB(B0, 0, 0); PG8_SCHED; PG8_LDA(At, 0, 0); PG8_STAGE(PG8_SA(1, 1), a1, voffA[1]);
;             PG8_WAIT_L(8); PG8_BAR; PG8_WAIT_L(0); PG8_MMA(0, 0, At, B0); PG8_BAR; PG8_SCHED;
;             if (last && has_next) PG8_AOFF(nxt);
;     ...
; #pragma unroll
;         for (int a = 0; a < 2; ++a)
; #pragma unroll
;             for (int b = 0; b < 2; ++b)
; #pragma unroll
;                 for (int m = 0; m < 4; ++m)
; #pragma unroll
;                     for (int n = 0; n < 2; ++n) acc[a][b][m][n] = (f32x4){0.f, 0.f, 0.f, 0.f};
;         cur = nxt; cB = nB; ++ui;
.LBB0_1001:
	s_ashr_i32 s11, s10, 31
	s_ashr_i32 s17, s16, 31
	s_xor_b64 s[20:21], s[24:25], -1
	s_lshl_b64 s[18:19], s[10:11], 19
	s_lshl_b64 s[28:29], s[16:17], 1
	s_add_u32 s11, s38, s18
	s_addc_u32 s17, s39, s19
	s_add_u32 s18, s11, s28
	s_addc_u32 s19, s17, s29
	s_and_b64 s[28:29], s[24:25], exec
	s_cselect_b32 s11, s19, s27
	s_cselect_b32 s17, s18, s26
	s_add_u32 s23, s26, 0x100
	v_mov_b32_e32 v2, 0
	s_addc_u32 s58, s27, 0
	s_add_i32 s59, s57, -2
	s_mov_b32 s60, 0
	s_mov_b64 s[26:27], 0
	v_mov_b32_e32 v3, v2
	v_mov_b64_e32 v[4:5], 0
	v_mov_b64_e32 v[6:7], 0
	v_mov_b64_e32 v[8:9], 0
	v_mov_b64_e32 v[10:11], 0
	v_mov_b64_e32 v[12:13], 0
	v_mov_b64_e32 v[14:15], 0
	v_mov_b64_e32 v[16:17], 0
	v_mov_b64_e32 v[22:23], 0
	v_mov_b64_e32 v[24:25], 0
	v_mov_b64_e32 v[30:31], 0
	v_mov_b64_e32 v[32:33], 0
	v_mov_b64_e32 v[38:39], 0
	v_mov_b64_e32 v[40:41], 0
	v_mov_b64_e32 v[46:47], 0
	v_mov_b64_e32 v[48:49], 0
	v_mov_b64_e32 v[18:19], 0
	v_mov_b64_e32 v[20:21], 0
	v_mov_b64_e32 v[26:27], 0
	v_mov_b64_e32 v[28:29], 0
	v_mov_b64_e32 v[34:35], 0
	v_mov_b64_e32 v[36:37], 0
	v_mov_b64_e32 v[42:43], 0
	v_mov_b64_e32 v[44:45], 0
	v_mov_b64_e32 v[50:51], 0
	v_mov_b64_e32 v[52:53], 0
	v_mov_b64_e32 v[54:55], 0
	v_mov_b64_e32 v[56:57], 0
	v_mov_b64_e32 v[58:59], 0
	v_mov_b64_e32 v[60:61], 0
	v_mov_b64_e32 v[62:63], 0
	v_mov_b64_e32 v[64:65], 0
	v_mov_b64_e32 v[66:67], 0
	s_waitcnt vmcnt(0)
	v_mov_b64_e32 v[68:69], 0
	v_mov_b64_e32 v[70:71], 0
	v_mov_b64_e32 v[72:73], 0
	v_mov_b64_e32 v[74:75], 0
	v_mov_b64_e32 v[76:77], 0
	v_mov_b64_e32 v[78:79], 0
	v_mov_b64_e32 v[80:81], 0
	v_mov_b64_e32 v[82:83], 0
	v_mov_b64_e32 v[84:85], 0
	v_mov_b64_e32 v[86:87], 0
	v_mov_b64_e32 v[88:89], 0
	v_mov_b64_e32 v[90:91], 0
	v_mov_b64_e32 v[92:93], 0
	v_mov_b64_e32 v[94:95], 0
	v_mov_b64_e32 v[96:97], 0
	v_mov_b64_e32 v[98:99], 0
	v_mov_b64_e32 v[100:101], 0
	v_mov_b64_e32 v[102:103], 0
	v_mov_b64_e32 v[104:105], 0
	v_mov_b64_e32 v[106:107], 0
	v_mov_b64_e32 v[108:109], 0
	v_mov_b64_e32 v[110:111], 0
	v_mov_b64_e32 v[112:113], 0
	v_mov_b64_e32 v[114:115], 0
	v_mov_b64_e32 v[116:117], 0
	v_mov_b64_e32 v[118:119], 0
	v_mov_b64_e32 v[120:121], 0
	v_mov_b64_e32 v[122:123], 0
	v_mov_b64_e32 v[124:125], 0
	v_mov_b64_e32 v[126:127], 0
	v_mov_b64_e32 v[128:129], 0
	s_cmp_lt_u32 s74, 0x100
	s_cbranch_scc1 .Lz1
	s_cmp_eq_u32 s100, 0
	s_cbranch_scc1 .Lz1
	s_barrier
.Lz1:
.LBB0_1002:
	v_add_u32_e32 v130, 0, v194
	v_add_u32_e32 v142, 0x10000, v130
	ds_read_b128 v[130:133], v142
	ds_read_b128 v[134:137], v142 offset:1024
	ds_read_b128 v[138:141], v142 offset:2048
	ds_read_b128 v[142:145], v142 offset:3072
	s_cmp_eq_u32 s59, s60
	s_cselect_b64 s[30:31], -1, 0
	s_add_i32 m0, s42, 0xc000
	s_add_u32 s28, s6, s26
	s_addc_u32 s29, s7, s27
	ds_read_b128 v[170:173], v195
	ds_read_b128 v[174:177], v195 offset:1024
	ds_read_b128 v[162:165], v195 offset:2048
	ds_read_b128 v[166:169], v195 offset:3072
	ds_read_b128 v[154:157], v195 offset:4096
	ds_read_b128 v[158:161], v195 offset:5120
	ds_read_b128 v[146:149], v195 offset:6144
	ds_read_b128 v[150:153], v195 offset:7168
	global_load_lds_dwordx4 v182, s[28:29]
	s_add_i32 m0, s42, 0xe000
	s_nop 0
	global_load_lds_dwordx4 v186, s[28:29]
	s_waitcnt lgkmcnt(8)
	s_barrier
	s_waitcnt lgkmcnt(0)
	s_waitcnt lgkmcnt(0)
	v_mfma_f32_16x16x32_bf16 v[126:129], v[130:133], v[170:173], v[126:129]
	v_mfma_f32_16x16x32_bf16 v[122:125], v[138:141], v[170:173], v[122:125]
	v_mfma_f32_16x16x32_bf16 v[118:121], v[130:133], v[162:165], v[118:121]
	v_mfma_f32_16x16x32_bf16 v[114:117], v[138:141], v[162:165], v[114:117]
	v_mfma_f32_16x16x32_bf16 v[110:113], v[130:133], v[154:157], v[110:113]
	v_mfma_f32_16x16x32_bf16 v[106:109], v[138:141], v[154:157], v[106:109]
	v_mfma_f32_16x16x32_bf16 v[102:105], v[130:133], v[146:149], v[102:105]
	v_mfma_f32_16x16x32_bf16 v[98:101], v[138:141], v[146:149], v[98:101]
	v_mfma_f32_16x16x32_bf16 v[126:129], v[134:137], v[174:177], v[126:129]
	v_mfma_f32_16x16x32_bf16 v[122:125], v[142:145], v[174:177], v[122:125]
	v_mfma_f32_16x16x32_bf16 v[118:121], v[134:137], v[166:169], v[118:121]
	v_mfma_f32_16x16x32_bf16 v[114:117], v[142:145], v[166:169], v[114:117]
	v_mfma_f32_16x16x32_bf16 v[110:113], v[134:137], v[158:161], v[110:113]
	v_mfma_f32_16x16x32_bf16 v[106:109], v[142:145], v[158:161], v[106:109]
	v_mfma_f32_16x16x32_bf16 v[102:105], v[134:137], v[150:153], v[102:105]
	v_mfma_f32_16x16x32_bf16 v[98:101], v[142:145], v[150:153], v[98:101]
	s_barrier
	s_and_b64 s[28:29], s[24:25], s[30:31]
	s_andn2_b64 vcc, exec, s[28:29]
	s_cbranch_vccnz .LBB0_1004
	v_mbcnt_lo_u32_b32 v0, -1, 0
	v_mbcnt_hi_u32_b32 v0, -1, v0
	s_nop 0
	v_or_b32_e32 v0, s75, v0
	v_ashrrev_i32_e32 v183, 31, v0
	v_lshrrev_b32_e32 v183, 26, v183
	v_lshlrev_b32_e32 v182, 4, v0
	v_add_u32_e32 v183, v0, v183
	v_bfe_i32 v0, v0, 27, 1
	v_lshrrev_b32_e32 v0, 22, v0
	v_add_u32_e32 v0, v182, v0
	v_and_b32_e32 v0, 0xfffffc00, v0
	v_sub_u32_e32 v0, v182, v0
	v_lshrrev_b32_e32 v184, 4, v0
	v_bitop3_b32 v0, v184, v0, 32 bitop3:0x6c
	v_ashrrev_i32_e32 v185, 31, v0
	v_lshrrev_b32_e32 v185, 26, v185
	v_add_u32_e32 v185, v0, v185
	v_ashrrev_i32_e32 v183, 6, v183
	v_lshrrev_b32_e32 v186, 6, v185
	v_and_b32_e32 v185, 0xc0, v185
	v_lshlrev_b32_e32 v184, 3, v183
	v_sub_u32_e32 v0, v0, v185
	v_and_b32_e32 v184, 0x1ffff0, v184
	v_lshlrev_b32_e32 v183, 5, v183
	v_ashrrev_i16_sdwa v0, v216, sext(v0) dst_sel:DWORD dst_unused:UNUSED_PAD src0_sel:DWORD src1_sel:BYTE_0
	v_and_b32_e32 v183, 32, v183
	v_bfe_i32 v0, v0, 0, 16
	v_add_u32_e32 v184, s55, v184
	v_add_u32_e32 v182, 0x2000, v182
	v_add3_u32 v0, v183, s16, v0
	v_add_lshl_u32 v183, v184, v186, 11
	v_ashrrev_i32_e32 v184, 31, v182
	v_lshrrev_b32_e32 v184, 22, v184
	v_add_u32_e32 v184, v182, v184
	v_ashrrev_i32_e32 v184, 10, v184
	v_mul_i32_i24_e32 v185, 0x400, v184
	v_sub_u32_e32 v182, v182, v185
	v_lshrrev_b32_e32 v185, 4, v182
	v_bitop3_b32 v182, v185, v182, 32 bitop3:0x6c
	v_ashrrev_i32_e32 v186, 31, v182
	v_lshrrev_b32_e32 v186, 26, v186
	v_add_u32_e32 v186, v182, v186
	v_lshrrev_b32_e32 v187, 6, v186
	v_and_b32_e32 v186, 0xc0, v186
	v_lshlrev_b32_e32 v185, 3, v184
	v_sub_u32_e32 v182, v182, v186
	v_and_b32_e32 v185, 0x1ffff0, v185
	v_lshlrev_b32_e32 v184, 5, v184
	v_ashrrev_i16_sdwa v182, v216, sext(v182) dst_sel:DWORD dst_unused:UNUSED_PAD src0_sel:DWORD src1_sel:BYTE_0
	v_and_b32_e32 v184, 32, v184
	v_bfe_i32 v182, v182, 0, 16
	v_add_u32_e32 v185, s55, v185
	v_lshl_add_u32 v183, v0, 1, v183
	v_add3_u32 v182, v184, s16, v182
	v_add_lshl_u32 v184, v185, v187, 11
	v_add_u32_e32 v0, 0x40000, v183
	v_lshl_add_u32 v184, v182, 1, v184
	v_add_u32_e32 v186, 0x40000, v184
	v_mov_b32_e32 v187, v1
	v_mov_b64_e32 v[192:193], v[0:1]
	v_mov_b32_e32 v182, v0
	v_mov_b32_e32 v0, v183
	s_branch .LBB0_1005

; template <class Epi, class Sched>
; __device__ __forceinline__ void gemm_phase(LAS unsigned char* lds, const bf16_t* Abase, const int K, const Sched& S, const Epi& E, const int wvid) {
;     ...
;         E(acc, cur, wr, wc, fr, fq);
;         if (!has_next) break;
; #pragma unroll
;         for (int a = 0; a < 2; ++a)
; #pragma unroll
;             for (int b = 0; b < 2; ++b)
; #pragma unroll
;                 for (int m = 0; m < 4; ++m)
; #pragma unroll
;                     for (int n = 0; n < 2; ++n) acc[a][b][m][n] = (f32x4){0.f, 0.f, 0.f, 0.f};
;         cur = nxt; cB = nB; ++ui;
.LBB0_1201:
	s_or_b64 exec, exec, s[0:1]
	s_mov_b32 s100, 1
	s_and_b64 vcc, exec, s[2:3]
	v_mov_b32_e32 v228, v227
	s_mov_b32 s24, s22
	v_mov_b32_e32 v179, v193
	v_mov_b64_e32 v[2:3], v[194:195]
	s_cbranch_vccnz .LBB0_1230

;     __device__ __forceinline__ const char* b_ptr(const Unit& u) const { return (const char*)Bt + ((size_t)u.pn * BM * K + u.koff) * 2; }
;     __device__ __forceinline__ const char* b_ptr(const Unit& u) const { return (const char*)Bt + ((size_t)u.e * bstride + (size_t)u.pn * BM * K) * 2; }
; template <class Epi, class Sched>
; __device__ __forceinline__ void gemm_phase(LAS unsigned char* lds, const bf16_t* Abase, const int K, const Sched& S, const Epi& E, const int wvid) {
;     ...
;         const bool has_next = S.next(ui + 1, nxt);
;         const char* nB = has_next ? S.b_ptr(nxt) : cB;
;         const int nt = cur.kt;
;     ...
; #pragma unroll
;         for (int a = 0; a < 2; ++a)
; #pragma unroll
;             for (int b = 0; b < 2; ++b)
; #pragma unroll
;                 for (int m = 0; m < 4; ++m)
; #pragma unroll
;                     for (int n = 0; n < 2; ++n) acc[a][b][m][n] = (f32x4){0.f, 0.f, 0.f, 0.f};
;         cur = nxt; cB = nB; ++ui;
.LBB0_1208:
	s_ashr_i32 s23, s22, 31
	s_lshl_b64 s[4:5], s[22:23], 19
	v_ashrrev_i32_e32 v191, 31, v190
	s_add_u32 s4, s36, s4
	v_lshlrev_b64 v[4:5], 21, v[190:191]
	s_addc_u32 s5, s37, s5
	v_lshl_add_u64 v[194:195], s[4:5], 0, v[4:5]
	s_mov_b64 s[4:5], 0x100
	v_cndmask_b32_e64 v229, v2, v194, s[0:1]
	v_lshl_add_u64 v[196:197], v[2:3], 0, s[4:5]
	v_mov_b32_e32 v2, 0
	v_cndmask_b32_e64 v191, v3, v195, s[0:1]
	v_add_u32_e32 v230, -1, v193
	v_add_u32_e32 v231, 0x80, v227
	s_mov_b32 s23, -2
	s_mov_b64 s[26:27], 0
	v_mov_b32_e32 v3, v2
	v_mov_b64_e32 v[4:5], 0
	v_mov_b64_e32 v[6:7], 0
	v_mov_b64_e32 v[8:9], 0
	v_mov_b64_e32 v[18:19], 0
	v_mov_b64_e32 v[20:21], 0
	v_mov_b64_e32 v[22:23], 0
	v_mov_b64_e32 v[24:25], 0
	v_mov_b64_e32 v[34:35], 0
	v_mov_b64_e32 v[36:37], 0
	v_mov_b64_e32 v[38:39], 0
	v_mov_b64_e32 v[40:41], 0
	v_mov_b64_e32 v[50:51], 0
	v_mov_b64_e32 v[52:53], 0
	v_mov_b64_e32 v[54:55], 0
	v_mov_b64_e32 v[56:57], 0
	v_mov_b64_e32 v[10:11], 0
	v_mov_b64_e32 v[12:13], 0
	v_mov_b64_e32 v[14:15], 0
	v_mov_b64_e32 v[16:17], 0
	v_mov_b64_e32 v[26:27], 0
	v_mov_b64_e32 v[28:29], 0
	v_mov_b64_e32 v[30:31], 0
	v_mov_b64_e32 v[32:33], 0
	v_mov_b64_e32 v[42:43], 0
	v_mov_b64_e32 v[44:45], 0
	v_mov_b64_e32 v[46:47], 0
	v_mov_b64_e32 v[48:49], 0
	v_mov_b64_e32 v[58:59], 0
	v_mov_b64_e32 v[60:61], 0
	v_mov_b64_e32 v[62:63], 0
	v_mov_b64_e32 v[64:65], 0
	v_mov_b64_e32 v[66:67], 0
	v_mov_b64_e32 v[68:69], 0
	v_mov_b64_e32 v[70:71], 0
	v_mov_b64_e32 v[72:73], 0
	v_mov_b64_e32 v[74:75], 0
	v_mov_b64_e32 v[76:77], 0
	v_mov_b64_e32 v[78:79], 0
	v_mov_b64_e32 v[80:81], 0
	v_mov_b64_e32 v[82:83], 0
	v_mov_b64_e32 v[84:85], 0
	v_mov_b64_e32 v[86:87], 0
	v_mov_b64_e32 v[88:89], 0
	v_mov_b64_e32 v[98:99], 0
	v_mov_b64_e32 v[100:101], 0
	v_mov_b64_e32 v[102:103], 0
	v_mov_b64_e32 v[104:105], 0
	v_mov_b64_e32 v[90:91], 0
	v_mov_b64_e32 v[92:93], 0
	v_mov_b64_e32 v[94:95], 0
	v_mov_b64_e32 v[96:97], 0
	v_mov_b64_e32 v[106:107], 0
	v_mov_b64_e32 v[108:109], 0
	v_mov_b64_e32 v[110:111], 0
	v_mov_b64_e32 v[112:113], 0
	v_mov_b64_e32 v[114:115], 0
	v_mov_b64_e32 v[116:117], 0
	v_mov_b64_e32 v[118:119], 0
	v_mov_b64_e32 v[120:121], 0
	v_mov_b64_e32 v[122:123], 0
	v_mov_b64_e32 v[124:125], 0
	v_mov_b64_e32 v[126:127], 0
	v_mov_b64_e32 v[128:129], 0
	s_cmp_lt_u32 s74, 0x100
	s_cbranch_scc1 .Lz2
	s_cmp_eq_u32 s100, 0
	s_cbranch_scc1 .Lz2
	s_barrier
; #define PG8_STAGE(bufoff, gbase, voff) do { _Pragma("unroll") for (int _i = 0; _i < 2; ++_i) \
;         __builtin_amdgcn_global_load_lds((const unsigned*)((const char*)(gbase) + (voff)[_i]), (LAS unsigned*)(lds + (bufoff) + ldsw + _i * 8192), 16, 0, 0); } while (0)
; #define PG8_LDA(dst, b, h) do { _Pragma("unroll") for (int m = 0; m < 4; ++m) _Pragma("unroll") for (int k = 0; k < 2; ++k) dst[m][k] = *(const LAS bf16x8*)(lds + PG8_SA(b, h) + aoff + m * 2048 + k * 1024); } while (0)
; #define PG8_LDB(dst, b, h) do { _Pragma("unroll") for (int n = 0; n < 2; ++n) _Pragma("unroll") for (int k = 0; k < 2; ++k) dst[n][k] = *(const LAS bf16x8*)(lds + PG8_SB(b, h) + boff + n * 2048 + k * 1024); } while (0)
; #define PG8_MMA(ai, bj, At, Bt) do { __builtin_amdgcn_s_setprio(1); _Pragma("unroll") for (int m = 0; m < 4; ++m) _Pragma("unroll") for (int n = 0; n < 2; ++n) _Pragma("unroll") for (int k = 0; k < 2; ++k) \
;         acc[ai][bj][m][n] = __builtin_amdgcn_mfma_f32_16x16x32_bf16(Bt[n][k], At[m][k], acc[ai][bj][m][n], 0, 0, 0); __builtin_amdgcn_s_setprio(0); } while (0)
; #define PG8_WAIT_L(n) asm volatile("s_waitcnt lgkmcnt(" #n ")" ::: "memory")
; #define PG8_BAR __builtin_amdgcn_s_barrier()
; #define PG8_SCHED __builtin_amdgcn_sched_barrier(0)
; #define PG8_AOFF(u) do { const int _t = lt_tid(wvid); _Pragma("unroll") for (int _i = 0; _i < 2; ++_i) { int _R, _C; stage_rc(_t * 16 + _i * 8192, _R, _C); \
;         _Pragma("unroll") for (int _h = 0; _h < 2; ++_h) voffA[_h][_i] = (S.a_row(u, _h * HALF + _R) * (unsigned)K + (unsigned)(_C + (u).koff)) * 2u; } } while (0)
; template <class Epi, class Sched>
; __device__ __forceinline__ void gemm_phase(LAS unsigned char* lds, const bf16_t* Abase, const int K, const Sched& S, const Epi& E, const int wvid) {
;     ...
;             PG8_LDB(B0, 0, 0); PG8_SCHED; PG8_LDA(At, 0, 0); PG8_STAGE(PG8_SA(1, 1), a1, voffA[1]);
;             PG8_WAIT_L(8); PG8_BAR; PG8_WAIT_L(0); PG8_MMA(0, 0, At, B0); PG8_BAR; PG8_SCHED;
;             if (last && has_next) PG8_AOFF(nxt);
.Lz2:
.LBB0_1209:
	v_add_u32_e32 v130, 0, v224
	v_add_u32_e32 v142, 0x10000, v130
	ds_read_b128 v[130:133], v142
	ds_read_b128 v[134:137], v142 offset:1024
	ds_read_b128 v[138:141], v142 offset:2048
	ds_read_b128 v[142:145], v142 offset:3072
	s_cmp_eq_u32 s23, 12
	s_cselect_b64 s[4:5], -1, 0
	s_add_i32 m0, s25, 0xc000
	s_add_u32 s28, s20, s26
	s_addc_u32 s29, s21, s27
	ds_read_b128 v[170:173], v226
	ds_read_b128 v[174:177], v226 offset:1024
	ds_read_b128 v[162:165], v226 offset:2048
	ds_read_b128 v[166:169], v226 offset:3072
	ds_read_b128 v[154:157], v226 offset:4096
	ds_read_b128 v[158:161], v226 offset:5120
	ds_read_b128 v[146:149], v226 offset:6144
	ds_read_b128 v[150:153], v226 offset:7168
	global_load_lds_dwordx4 v186, s[28:29]
	s_add_i32 m0, s25, 0xe000
	s_nop 0
	global_load_lds_dwordx4 v188, s[28:29]
	s_waitcnt lgkmcnt(8)
	s_barrier
	s_waitcnt lgkmcnt(0)
	s_waitcnt lgkmcnt(0)
	v_mfma_f32_16x16x32_bf16 v[126:129], v[130:133], v[170:173], v[126:129]
	v_mfma_f32_16x16x32_bf16 v[122:125], v[138:141], v[170:173], v[122:125]
	v_mfma_f32_16x16x32_bf16 v[118:121], v[130:133], v[162:165], v[118:121]
	v_mfma_f32_16x16x32_bf16 v[114:117], v[138:141], v[162:165], v[114:117]
	v_mfma_f32_16x16x32_bf16 v[110:113], v[130:133], v[154:157], v[110:113]
	v_mfma_f32_16x16x32_bf16 v[106:109], v[138:141], v[154:157], v[106:109]
	v_mfma_f32_16x16x32_bf16 v[94:97], v[130:133], v[146:149], v[94:97]
	v_mfma_f32_16x16x32_bf16 v[90:93], v[138:141], v[146:149], v[90:93]
	v_mfma_f32_16x16x32_bf16 v[126:129], v[134:137], v[174:177], v[126:129]
	v_mfma_f32_16x16x32_bf16 v[122:125], v[142:145], v[174:177], v[122:125]
	v_mfma_f32_16x16x32_bf16 v[118:121], v[134:137], v[166:169], v[118:121]
	v_mfma_f32_16x16x32_bf16 v[114:117], v[142:145], v[166:169], v[114:117]
	v_mfma_f32_16x16x32_bf16 v[110:113], v[134:137], v[158:161], v[110:113]
	v_mfma_f32_16x16x32_bf16 v[106:109], v[142:145], v[158:161], v[106:109]
	v_mfma_f32_16x16x32_bf16 v[94:97], v[134:137], v[150:153], v[94:97]
	v_mfma_f32_16x16x32_bf16 v[90:93], v[142:145], v[150:153], v[90:93]
	s_barrier
	s_and_b64 s[28:29], s[0:1], s[4:5]
	s_andn2_b64 vcc, exec, s[28:29]
	s_cbranch_vccnz .LBB0_1211
	v_mbcnt_lo_u32_b32 v0, -1, 0
	v_mbcnt_hi_u32_b32 v0, -1, v0
	v_mov_b32_e32 v189, v1
	v_or_b32_e32 v0, s75, v0
	v_ashrrev_i32_e32 v184, 31, v0
	v_lshrrev_b32_e32 v184, 26, v184
	v_lshlrev_b32_e32 v186, 4, v0
	v_add_u32_e32 v184, v0, v184
	v_bfe_i32 v0, v0, 27, 1
	v_lshrrev_b32_e32 v0, 22, v0
	v_add_u32_e32 v0, v186, v0
	v_and_b32_e32 v0, 0xfffffc00, v0
	v_sub_u32_e32 v0, v186, v0
	v_lshrrev_b32_e32 v185, 4, v0
	v_bitop3_b32 v0, v185, v0, 32 bitop3:0x6c
	v_ashrrev_i32_e32 v187, 31, v0
	v_ashrrev_i32_e32 v184, 6, v184
	v_lshrrev_b32_e32 v187, 26, v187
	v_lshlrev_b32_e32 v185, 3, v184
	v_add_u32_e32 v187, v0, v187
	v_and_b32_e32 v185, -16, v185
	v_ashrrev_i32_e32 v188, 6, v187
	v_add_u32_e32 v188, v188, v185
	v_and_b32_e32 v185, 0xc0, v187
	v_sub_u32_e32 v0, v0, v185
	v_lshlrev_b32_e32 v184, 5, v184
	v_ashrrev_i16_sdwa v0, v216, sext(v0) dst_sel:DWORD dst_unused:UNUSED_PAD src0_sel:DWORD src1_sel:BYTE_0
	v_and_b32_e32 v184, 32, v184
	v_bfe_i32 v0, v0, 0, 16
	v_add_lshl_u32 v0, v184, v0, 1
	v_add_u32_e32 v232, v188, v227
	v_min_i32_e32 v232, v232, v230
	v_add_u32_e32 v232, v232, v192
	v_ashrrev_i32_e32 v233, 31, v232
	v_lshl_add_u64 v[232:233], v[232:233], 2, s[10:11]
	global_load_dword v240, v[232:233], off
	v_add_u32_e32 v234, v188, v231
	v_min_i32_e32 v234, v234, v230
	v_add_u32_e32 v234, v234, v192
	v_ashrrev_i32_e32 v235, 31, v234
	v_lshl_add_u64 v[234:235], v[234:235], 2, s[10:11]
	global_load_dword v241, v[234:235], off
	v_add_u32_e32 v184, 0x2000, v186
	v_ashrrev_i32_e32 v185, 31, v184
	v_lshrrev_b32_e32 v185, 22, v185
	v_add_u32_e32 v185, v184, v185
	v_ashrrev_i32_e32 v185, 10, v185
	v_mul_i32_i24_e32 v186, 0x400, v185
	v_sub_u32_e32 v184, v184, v186
	v_lshrrev_b32_e32 v186, 4, v184
	v_bitop3_b32 v184, v186, v184, 32 bitop3:0x6c
	v_ashrrev_i32_e32 v187, 31, v184
	v_lshrrev_b32_e32 v187, 26, v187
	v_add_u32_e32 v187, v184, v187
	v_ashrrev_i32_e32 v188, 6, v187
	v_and_b32_e32 v187, 0xc0, v187
	v_lshlrev_b32_e32 v186, 3, v185
	v_sub_u32_e32 v184, v184, v187
	v_and_b32_e32 v186, -16, v186
	v_lshlrev_b32_e32 v185, 5, v185
	v_ashrrev_i16_sdwa v184, v216, sext(v184) dst_sel:DWORD dst_unused:UNUSED_PAD src0_sel:DWORD src1_sel:BYTE_0
	v_add_u32_e32 v186, v188, v186
	v_and_b32_e32 v185, 32, v185
	v_bfe_i32 v184, v184, 0, 16
	v_add_lshl_u32 v188, v185, v184, 1
	v_add_u32_e32 v236, v186, v227
	v_min_i32_e32 v236, v236, v230
	v_add_u32_e32 v236, v236, v192
	v_ashrrev_i32_e32 v237, 31, v236
	v_lshl_add_u64 v[236:237], v[236:237], 2, s[10:11]
	global_load_dword v242, v[236:237], off
	v_add_u32_e32 v238, v186, v231
	v_min_i32_e32 v238, v238, v230
	v_add_u32_e32 v238, v238, v192
	v_ashrrev_i32_e32 v239, 31, v238
	v_lshl_add_u64 v[238:239], v[238:239], 2, s[10:11]
	global_load_dword v243, v[238:239], off
	s_waitcnt vmcnt(0)
	v_lshl_add_u32 v200, v240, 11, v0
	v_lshl_add_u32 v0, v241, 11, v0
	v_mov_b64_e32 v[198:199], v[0:1]
	v_mov_b32_e32 v186, v0
	v_mov_b32_e32 v0, v200
	v_lshl_add_u32 v184, v242, 11, v188
	v_lshl_add_u32 v188, v243, 11, v188
	s_branch .LBB0_1212

; #define PG8_WAIT_V(n) asm volatile("s_waitcnt vmcnt(" #n ")" ::: "memory")
; #define PG8_BAR __builtin_amdgcn_s_barrier()
; template <class Epi, class Sched>
; __device__ __forceinline__ void gemm_phase(LAS unsigned char* lds, const bf16_t* Abase, const int K, const Sched& S, const Epi& E, const int wvid) {
;     ...
;     PG8_WAIT_V(0);
;     if (wr == 0) PG8_BAR;
;     PG8_BAR;
.Lw2:
	s_mov_b32 s100, 0
	s_waitcnt vmcnt(0)
	s_cmpk_gt_u32 s35, 0xff
	s_cbranch_scc1 .LBB0_1232
	s_barrier

; template <class Epi, class Sched>
; __device__ __forceinline__ void gemm_phase(LAS unsigned char* lds, const bf16_t* Abase, const int K, const Sched& S, const Epi& E, const int wvid) {
;     ...
;         E(acc, cur, wr, wc, fr, fq);
;         if (!has_next) break;
; #pragma unroll
;         for (int a = 0; a < 2; ++a)
; #pragma unroll
;             for (int b = 0; b < 2; ++b)
; #pragma unroll
;                 for (int m = 0; m < 4; ++m)
; #pragma unroll
;                     for (int n = 0; n < 2; ++n) acc[a][b][m][n] = (f32x4){0.f, 0.f, 0.f, 0.f};
;         cur = nxt; cB = nB; ++ui;
.LBB0_1468:
	s_or_b64 exec, exec, s[0:1]
	s_mov_b32 s100, 1
	s_and_b64 vcc, exec, s[2:3]
	v_mov_b32_e32 v227, v228
	s_mov_b32 s16, s24
	v_mov_b32_e32 v179, v193
	v_mov_b32_e32 v226, v192
	v_mov_b64_e32 v[2:3], v[194:195]
	s_cbranch_vccnz .LBB0_1497

;     __device__ __forceinline__ const char* b_ptr(const Unit& u) const { return (const char*)Bt + ((size_t)u.pn * BM * K + u.koff) * 2; }
;     __device__ __forceinline__ const char* b_ptr(const Unit& u) const { return (const char*)Bt + ((size_t)u.e * bstride + (size_t)u.pn * BM * K) * 2; }
; #define PG8_STAGE(bufoff, gbase, voff) do { _Pragma("unroll") for (int _i = 0; _i < 2; ++_i) \
;         __builtin_amdgcn_global_load_lds((const unsigned*)((const char*)(gbase) + (voff)[_i]), (LAS unsigned*)(lds + (bufoff) + ldsw + _i * 8192), 16, 0, 0); } while (0)
; #define PG8_LDA(dst, b, h) do { _Pragma("unroll") for (int m = 0; m < 4; ++m) _Pragma("unroll") for (int k = 0; k < 2; ++k) dst[m][k] = *(const LAS bf16x8*)(lds + PG8_SA(b, h) + aoff + m * 2048 + k * 1024); } while (0)
; #define PG8_LDB(dst, b, h) do { _Pragma("unroll") for (int n = 0; n < 2; ++n) _Pragma("unroll") for (int k = 0; k < 2; ++k) dst[n][k] = *(const LAS bf16x8*)(lds + PG8_SB(b, h) + boff + n * 2048 + k * 1024); } while (0)
; #define PG8_WAIT_L(n) asm volatile("s_waitcnt lgkmcnt(" #n ")" ::: "memory")
; #define PG8_BAR __builtin_amdgcn_s_barrier()
; #define PG8_SCHED __builtin_amdgcn_sched_barrier(0)
; template <class Epi, class Sched>
; __device__ __forceinline__ void gemm_phase(LAS unsigned char* lds, const bf16_t* Abase, const int K, const Sched& S, const Epi& E, const int wvid) {
;     ...
;         const bool has_next = S.next(ui + 1, nxt);
;         const char* nB = has_next ? S.b_ptr(nxt) : cB;
;         const int nt = cur.kt;
;         for (int t = 0; t < nt; t += 2) {
;             const bool last = (t == nt - 2);
;             const char* a1 = Ab + (size_t)(t + 1) * kstep;
;             PG8_LDB(B0, 0, 0); PG8_SCHED; PG8_LDA(At, 0, 0); PG8_STAGE(PG8_SA(1, 1), a1, voffA[1]);
;             PG8_WAIT_L(8); PG8_BAR; PG8_WAIT_L(0); PG8_MMA(0, 0, At, B0); PG8_BAR; PG8_SCHED;
;             if (last && has_next) PG8_AOFF(nxt);
;     ...
; #pragma unroll
;         for (int a = 0; a < 2; ++a)
; #pragma unroll
;             for (int b = 0; b < 2; ++b)
; #pragma unroll
;                 for (int m = 0; m < 4; ++m)
; #pragma unroll
;                     for (int n = 0; n < 2; ++n) acc[a][b][m][n] = (f32x4){0.f, 0.f, 0.f, 0.f};
;         cur = nxt; cB = nB; ++ui;
.LBB0_1475:
	s_ashr_i32 s25, s24, 31
	s_lshl_b64 s[4:5], s[24:25], 18
	v_ashrrev_i32_e32 v191, 31, v190
	s_add_u32 s4, s36, s4
	v_lshlrev_b64 v[4:5], 20, v[190:191]
	s_addc_u32 s5, s37, s5
	v_lshl_add_u64 v[194:195], s[4:5], 0, v[4:5]
	s_mov_b64 s[4:5], 0x100
	v_cndmask_b32_e64 v229, v2, v194, s[0:1]
	v_lshl_add_u64 v[196:197], v[2:3], 0, s[4:5]
	v_mov_b32_e32 v2, 0
	v_cndmask_b32_e64 v191, v3, v195, s[0:1]
	v_add_u32_e32 v230, 0x80, v228
	s_mov_b32 s25, -2
	s_mov_b64 s[26:27], 0
	v_mov_b32_e32 v3, v2
	v_mov_b64_e32 v[4:5], 0
	v_mov_b64_e32 v[6:7], 0
	v_mov_b64_e32 v[8:9], 0
	v_mov_b64_e32 v[18:19], 0
	v_mov_b64_e32 v[20:21], 0
	v_mov_b64_e32 v[22:23], 0
	v_mov_b64_e32 v[24:25], 0
	v_mov_b64_e32 v[34:35], 0
	v_mov_b64_e32 v[36:37], 0
	v_mov_b64_e32 v[38:39], 0
	v_mov_b64_e32 v[40:41], 0
	v_mov_b64_e32 v[50:51], 0
	v_mov_b64_e32 v[52:53], 0
	v_mov_b64_e32 v[54:55], 0
	v_mov_b64_e32 v[56:57], 0
	v_mov_b64_e32 v[10:11], 0
	v_mov_b64_e32 v[12:13], 0
	v_mov_b64_e32 v[14:15], 0
	v_mov_b64_e32 v[16:17], 0
	v_mov_b64_e32 v[26:27], 0
	v_mov_b64_e32 v[28:29], 0
	v_mov_b64_e32 v[30:31], 0
	v_mov_b64_e32 v[32:33], 0
	v_mov_b64_e32 v[42:43], 0
	v_mov_b64_e32 v[44:45], 0
	v_mov_b64_e32 v[46:47], 0
	v_mov_b64_e32 v[48:49], 0
	v_mov_b64_e32 v[58:59], 0
	v_mov_b64_e32 v[60:61], 0
	v_mov_b64_e32 v[62:63], 0
	v_mov_b64_e32 v[64:65], 0
	v_mov_b64_e32 v[66:67], 0
	v_mov_b64_e32 v[68:69], 0
	v_mov_b64_e32 v[70:71], 0
	v_mov_b64_e32 v[72:73], 0
	v_mov_b64_e32 v[74:75], 0
	v_mov_b64_e32 v[76:77], 0
	v_mov_b64_e32 v[78:79], 0
	v_mov_b64_e32 v[80:81], 0
	v_mov_b64_e32 v[82:83], 0
	v_mov_b64_e32 v[84:85], 0
	v_mov_b64_e32 v[86:87], 0
	v_mov_b64_e32 v[88:89], 0
	v_mov_b64_e32 v[90:91], 0
	v_mov_b64_e32 v[92:93], 0
	v_mov_b64_e32 v[94:95], 0
	v_mov_b64_e32 v[96:97], 0
	v_mov_b64_e32 v[98:99], 0
	v_mov_b64_e32 v[100:101], 0
	v_mov_b64_e32 v[102:103], 0
	v_mov_b64_e32 v[104:105], 0
	v_mov_b64_e32 v[106:107], 0
	v_mov_b64_e32 v[108:109], 0
	v_mov_b64_e32 v[110:111], 0
	v_mov_b64_e32 v[112:113], 0
	v_mov_b64_e32 v[114:115], 0
	v_mov_b64_e32 v[116:117], 0
	v_mov_b64_e32 v[118:119], 0
	v_mov_b64_e32 v[120:121], 0
	v_mov_b64_e32 v[122:123], 0
	v_mov_b64_e32 v[124:125], 0
	v_mov_b64_e32 v[126:127], 0
	v_mov_b64_e32 v[128:129], 0
	s_cmp_lt_u32 s74, 0x100
	s_cbranch_scc1 .Lz3
	s_cmp_eq_u32 s100, 0
	s_cbranch_scc1 .Lz3
	s_barrier
.Lz3:
.LBB0_1476:
	s_waitcnt vmcnt(0)
	v_add_u32_e32 v130, 0, v223
	v_add_u32_e32 v142, 0x10000, v130
	ds_read_b128 v[130:133], v142
	ds_read_b128 v[134:137], v142 offset:1024
	ds_read_b128 v[138:141], v142 offset:2048
	ds_read_b128 v[142:145], v142 offset:3072
	s_cmp_eq_u32 s25, 4
	s_cselect_b64 s[4:5], -1, 0
	s_add_i32 m0, s17, 0xc000
	s_add_u32 s28, s22, s26
	s_addc_u32 s29, s23, s27
	ds_read_b128 v[170:173], v225
	ds_read_b128 v[174:177], v225 offset:1024
	ds_read_b128 v[162:165], v225 offset:2048
	ds_read_b128 v[166:169], v225 offset:3072
	ds_read_b128 v[154:157], v225 offset:4096
	ds_read_b128 v[158:161], v225 offset:5120
	ds_read_b128 v[146:149], v225 offset:6144
	ds_read_b128 v[150:153], v225 offset:7168
	global_load_lds_dwordx4 v184, s[28:29]
	s_add_i32 m0, s17, 0xe000
	s_nop 0
	global_load_lds_dwordx4 v188, s[28:29]
	s_waitcnt lgkmcnt(8)
	s_barrier
	s_waitcnt lgkmcnt(0)
	s_waitcnt lgkmcnt(0)
	v_mfma_f32_16x16x32_bf16 v[126:129], v[130:133], v[170:173], v[126:129]
	v_mfma_f32_16x16x32_bf16 v[122:125], v[138:141], v[170:173], v[122:125]
	v_mfma_f32_16x16x32_bf16 v[118:121], v[130:133], v[162:165], v[118:121]
	v_mfma_f32_16x16x32_bf16 v[114:117], v[138:141], v[162:165], v[114:117]
	v_mfma_f32_16x16x32_bf16 v[110:113], v[130:133], v[154:157], v[110:113]
	v_mfma_f32_16x16x32_bf16 v[106:109], v[138:141], v[154:157], v[106:109]
	v_mfma_f32_16x16x32_bf16 v[102:105], v[130:133], v[146:149], v[102:105]
	v_mfma_f32_16x16x32_bf16 v[98:101], v[138:141], v[146:149], v[98:101]
	v_mfma_f32_16x16x32_bf16 v[126:129], v[134:137], v[174:177], v[126:129]
	v_mfma_f32_16x16x32_bf16 v[122:125], v[142:145], v[174:177], v[122:125]
	v_mfma_f32_16x16x32_bf16 v[118:121], v[134:137], v[166:169], v[118:121]
	v_mfma_f32_16x16x32_bf16 v[114:117], v[142:145], v[166:169], v[114:117]
	v_mfma_f32_16x16x32_bf16 v[110:113], v[134:137], v[158:161], v[110:113]
	v_mfma_f32_16x16x32_bf16 v[106:109], v[142:145], v[158:161], v[106:109]
	v_mfma_f32_16x16x32_bf16 v[102:105], v[134:137], v[150:153], v[102:105]
	v_mfma_f32_16x16x32_bf16 v[98:101], v[142:145], v[150:153], v[98:101]
	s_barrier
	s_and_b64 s[28:29], s[0:1], s[4:5]
	s_andn2_b64 vcc, exec, s[28:29]
	s_cbranch_vccnz .LBB0_1478
	v_mbcnt_lo_u32_b32 v0, -1, 0
	v_mbcnt_hi_u32_b32 v0, -1, v0
	s_nop 0
	v_or_b32_e32 v0, s75, v0
	v_ashrrev_i32_e32 v185, 31, v0
	v_lshrrev_b32_e32 v185, 26, v185
	v_lshlrev_b32_e32 v184, 4, v0
	v_add_u32_e32 v185, v0, v185
	v_bfe_i32 v0, v0, 27, 1
	v_lshrrev_b32_e32 v0, 22, v0
	v_add_u32_e32 v0, v184, v0
	v_and_b32_e32 v0, 0xfffffc00, v0
	v_sub_u32_e32 v0, v184, v0
	v_lshrrev_b32_e32 v186, 4, v0
	v_bitop3_b32 v0, v186, v0, 32 bitop3:0x6c
	v_ashrrev_i32_e32 v187, 31, v0
	v_lshrrev_b32_e32 v187, 26, v187
	v_add_u32_e32 v187, v0, v187
	v_ashrrev_i32_e32 v185, 6, v185
	v_ashrrev_i32_e32 v188, 6, v187
	v_and_b32_e32 v187, 0xc0, v187
	v_lshlrev_b32_e32 v186, 3, v185
	v_sub_u32_e32 v0, v0, v187
	v_and_b32_e32 v186, -16, v186
	v_lshlrev_b32_e32 v185, 5, v185
	v_ashrrev_i16_sdwa v0, v216, sext(v0) dst_sel:DWORD dst_unused:UNUSED_PAD src0_sel:DWORD src1_sel:BYTE_0
	v_add_u32_e32 v186, v188, v186
	v_and_b32_e32 v185, 32, v185
	v_bfe_i32 v0, v0, 0, 16
	v_add_lshl_u32 v0, v185, v0, 1
	v_add_u32_e32 v185, v186, v228
	v_add_u32_e32 v186, v186, v230
	v_add_u32_e32 v184, 0x2000, v184
	v_lshl_add_u32 v185, v185, 10, v0
	v_lshl_add_u32 v0, v186, 10, v0
	v_ashrrev_i32_e32 v186, 31, v184
	v_lshrrev_b32_e32 v186, 22, v186
	v_add_u32_e32 v186, v184, v186
	v_ashrrev_i32_e32 v186, 10, v186
	v_mul_i32_i24_e32 v187, 0x400, v186
	v_sub_u32_e32 v184, v184, v187
	v_lshrrev_b32_e32 v187, 4, v184
	v_bitop3_b32 v184, v187, v184, 32 bitop3:0x6c
	v_ashrrev_i32_e32 v188, 31, v184
	v_lshrrev_b32_e32 v188, 26, v188
	v_add_u32_e32 v188, v184, v188
	v_ashrrev_i32_e32 v189, 6, v188
	v_and_b32_e32 v188, 0xc0, v188
	v_lshlrev_b32_e32 v187, 3, v186
	v_sub_u32_e32 v184, v184, v188
	v_and_b32_e32 v187, -16, v187
	v_lshlrev_b32_e32 v186, 5, v186
	v_ashrrev_i16_sdwa v184, v216, sext(v184) dst_sel:DWORD dst_unused:UNUSED_PAD src0_sel:DWORD src1_sel:BYTE_0
	v_add_u32_e32 v187, v189, v187
	v_and_b32_e32 v186, 32, v186
	v_bfe_i32 v184, v184, 0, 16
	v_add_lshl_u32 v184, v186, v184, 1
	v_add_u32_e32 v186, v187, v228
	v_add_u32_e32 v187, v187, v230
	v_lshl_add_u32 v186, v186, 10, v184
	v_lshl_add_u32 v188, v187, 10, v184
	v_mov_b32_e32 v189, v1
	v_mov_b64_e32 v[198:199], v[0:1]
	v_mov_b32_e32 v184, v0
	v_mov_b32_e32 v0, v185
	s_branch .LBB0_1479

; #define LAS __attribute__((address_space(3)))
; __global__ void __launch_bounds__(NTHR, 2) k_fused(Params p) {
;     extern __shared__ __attribute__((aligned(16))) unsigned char smem[];
;     LAS unsigned char* lds = (LAS unsigned char*)smem;
;     const int wvid = __builtin_amdgcn_readfirstlane((int)threadIdx.x >> 6);
;     volatile LAS unsigned* st = (volatile LAS unsigned*)(lds + LDS_BYTES - 16);
	.amdhsa_kernel _Z7k_fused6Params
		.amdhsa_group_segment_fixed_size 0
		.amdhsa_private_segment_fixed_size 0
		.amdhsa_kernarg_size 568
		.amdhsa_user_sgpr_count 2
		.amdhsa_user_sgpr_dispatch_ptr 0
		.amdhsa_user_sgpr_queue_ptr 0
		.amdhsa_user_sgpr_kernarg_segment_ptr 1
		.amdhsa_user_sgpr_dispatch_id 0
		.amdhsa_user_sgpr_kernarg_preload_length 0
		.amdhsa_user_sgpr_kernarg_preload_offset 0
		.amdhsa_user_sgpr_private_segment_size 0
		.amdhsa_uses_dynamic_stack 0
		.amdhsa_enable_private_segment 0
		.amdhsa_system_sgpr_workgroup_id_x 1
		.amdhsa_system_sgpr_workgroup_id_y 0
		.amdhsa_system_sgpr_workgroup_id_z 0
		.amdhsa_system_sgpr_workgroup_info 0
		.amdhsa_system_vgpr_workitem_id 0
		.amdhsa_next_free_vgpr 256
		.amdhsa_next_free_sgpr 102
		.amdhsa_accum_offset 256
		.amdhsa_reserve_vcc 1
		.amdhsa_float_round_mode_32 0
		.amdhsa_float_round_mode_16_64 0
		.amdhsa_float_denorm_mode_32 3
		.amdhsa_float_denorm_mode_16_64 3
		.amdhsa_dx10_clamp 1
		.amdhsa_ieee_mode 1
		.amdhsa_fp16_overflow 0
		.amdhsa_tg_split 0
		.amdhsa_exception_fp_ieee_invalid_op 0
		.amdhsa_exception_fp_denorm_src 0
		.amdhsa_exception_fp_ieee_div_zero 0
		.amdhsa_exception_fp_ieee_overflow 0
		.amdhsa_exception_fp_ieee_underflow 0
		.amdhsa_exception_fp_ieee_inexact 0
		.amdhsa_exception_int_div_zero 0
	.end_amdhsa_kernel

; #define LAS __attribute__((address_space(3)))
; __global__ void __launch_bounds__(NTHR, 2) k_fused(Params p) {
;     extern __shared__ __attribute__((aligned(16))) unsigned char smem[];
;     LAS unsigned char* lds = (LAS unsigned char*)smem;
;     const int wvid = __builtin_amdgcn_readfirstlane((int)threadIdx.x >> 6);
;     volatile LAS unsigned* st = (volatile LAS unsigned*)(lds + LDS_BYTES - 16);
amdhsa.kernels:
  - .agpr_count:     0
    .args:
      - .offset:         0
        .size:           312
        .value_kind:     by_value
      - .offset:         312
        .size:           4
        .value_kind:     hidden_block_count_x
      - .offset:         316
        .size:           4
        .value_kind:     hidden_block_count_y
      - .offset:         320
        .size:           4
        .value_kind:     hidden_block_count_z
      - .offset:         324
        .size:           2
        .value_kind:     hidden_group_size_x
      - .offset:         326
        .size:           2
        .value_kind:     hidden_group_size_y
      - .offset:         328
        .size:           2
        .value_kind:     hidden_group_size_z
      - .offset:         330
        .size:           2
        .value_kind:     hidden_remainder_x
      - .offset:         332
        .size:           2
        .value_kind:     hidden_remainder_y
      - .offset:         334
        .size:           2
        .value_kind:     hidden_remainder_z
      - .offset:         352
        .size:           8
        .value_kind:     hidden_global_offset_x
      - .offset:         360
        .size:           8
        .value_kind:     hidden_global_offset_y
      - .offset:         368
        .size:           8
        .value_kind:     hidden_global_offset_z
      - .offset:         376
        .size:           2
        .value_kind:     hidden_grid_dims
      - .offset:         432
        .size:           4
        .value_kind:     hidden_dynamic_lds_size
    .group_segment_fixed_size: 0
    .kernarg_segment_align: 8
    .kernarg_segment_size: 568
    .language:       OpenCL C
    .language_version:
      - 2
      - 0
    .max_flat_workgroup_size: 512
    .name:           _Z7k_fused6Params
    .private_segment_fixed_size: 0
    .sgpr_count:     108
    .sgpr_spill_count: 151
    .symbol:         _Z7k_fused6Params.kd
    .uniform_work_group_size: 1
    .uses_dynamic_stack: false
    .vgpr_count:     256
    .vgpr_spill_count: 0
    .wavefront_size: 64
